# attention phase: one static s_setprio 1 for waves 4-7 for the whole phase (reset at phase exit), on top of the previous stack
# speedup vs baseline: 1.0049x; 1.0049x over previous
.LBB0_2089:
	s_or_b64 exec, exec, s[8:9]
	s_waitcnt lgkmcnt(0)
	s_barrier
	s_load_dwordx2 s[0:1], s[90:91], 0xc8
	s_waitcnt vmcnt(1)
	v_lshrrev_b32_e32 v2, 1, v0
	v_and_b32_e32 v2, 6, v2
	v_and_b32_e32 v1, 3, v0
	v_lshlrev_b32_e32 v3, 3, v0
	s_waitcnt lgkmcnt(0)
	s_add_u32 s40, s0, 0x2ec00000
	s_addc_u32 s41, s1, 0
	s_add_u32 s42, s0, 0x36c00000
	s_addc_u32 s43, s1, 0
	s_add_u32 s44, s0, 0x3ec00000
	s_addc_u32 s45, s1, 0
	s_add_u32 s46, s0, 0x4fc00000
	s_addc_u32 s47, s1, 0
	s_add_u32 s48, s0, 0x1800000
	s_addc_u32 s49, s1, 0
	s_lshr_b32 s3, s57, 29
	s_add_i32 s3, s97, s3
	s_ashr_i32 s3, s3, 3
	s_mul_i32 s50, s3, s64
	v_readlane_b32 s3, v254, 12
	s_add_i32 s50, s50, s3
	v_add_u32_e32 v2, s50, v2
	v_and_b32_e32 v2, 7, v2
	v_mul_u32_u24_e32 v5, 3, v2
	v_add3_u32 v5, v5, v1, 4
	v_cmp_eq_u32_e32 vcc, 0, v1
	s_ashr_i32 s51, s50, 3
	v_and_b32_e32 v3, 0x60, v3
	v_lshl_or_b32 v4, v2, 2, v1
	v_cndmask_b32_e32 v1, v5, v2, vcc
	v_cmp_gt_u32_e32 vcc, 5, v2
	v_add_u32_e32 v3, s51, v3
	s_movk_i32 s22, 0xe000
	v_cndmask_b32_e32 v1, v4, v1, vcc
	v_lshl_add_u32 v2, v3, 5, v1
	v_ashrrev_i32_e32 v3, 31, v2
	v_lshl_add_u64 v[2:3], v[2:3], 2, s[0:1]
	s_mov_b32 s0, 0x420000
	v_add_co_u32_e32 v2, vcc, s0, v2
	s_mov_b32 s13, 0
	s_nop 0
	v_addc_co_u32_e32 v3, vcc, 0, v3, vcc
	global_load_dword v1, v[2:3], off
	v_mov_b32_e32 v3, 0
	s_mov_b64 s[14:15], 0x2000
	s_mov_b64 s[16:17], 0x4000
	s_add_i32 s69, 0, 0x14800
	s_movk_i32 s72, 0xc0
	s_mov_b64 s[18:19], 0x6000
	s_mov_b64 s[20:21], 0xa000
	s_add_i32 s73, 0, 0x14900
	s_mov_b32 s23, -1
	s_mov_b64 s[24:25], 0x8000
	s_mov_b32 s74, 0x42700000
	v_mov_b32_e32 v194, 0xff800000
	s_mov_b32 s75, 0
	v_readfirstlane_b32 s3, v0
	s_nop 3
	s_lshr_b32 s3, s3, 8
	s_cmp_lg_u32 s3, 0
	s_cbranch_scc0 .Lattn_prio_done
	s_setprio 1
.Lattn_prio_done:
	s_waitcnt vmcnt(0)
	s_branch .LBB0_2093

.LBB0_2234:
	s_setprio 0
	s_waitcnt vmcnt(0)
	s_barrier
	s_mov_b64 s[8:9], exec
	v_readlane_b32 s0, v254, 2
	v_readlane_b32 s1, v254, 3
	s_and_b64 s[0:1], s[8:9], s[0:1]
	s_mov_b64 exec, s[0:1]
	s_cbranch_execz .LBB0_2286
	s_add_i32 s0, 0, 0x25960
	s_waitcnt vmcnt(0)
	v_mov_b32_e32 v1, s0
	s_waitcnt vmcnt(0) expcnt(0) lgkmcnt(0)
	ds_read_b32 v3, v1
	s_add_i32 s0, 0, 0x25964
	v_mov_b32_e32 v1, s0
	ds_read_b32 v1, v1
	s_waitcnt lgkmcnt(1)
	v_cmp_ne_u32_e32 vcc, 0, v3
	s_cbranch_vccnz .LBB0_2250
	s_add_u32 s10, s52, 0x4200
	s_addc_u32 s11, s53, 0
	s_add_u32 s12, s52, 0x4400
	s_addc_u32 s13, s53, 0
	s_add_u32 s14, s52, 0x4500
	s_addc_u32 s15, s53, 0
	s_add_u32 s16, s52, 0x4600
	s_addc_u32 s17, s53, 0
	s_add_u32 s18, s52, 0x4700
	s_addc_u32 s19, s53, 0
	s_add_u32 s20, s52, 0x4800
	s_addc_u32 s21, s53, 0
	s_add_u32 s22, s52, 0x4900
	s_addc_u32 s23, s53, 0
	s_add_u32 s24, s52, 0x4a00
	s_addc_u32 s25, s53, 0
	s_add_u32 s26, s52, 0x4b00
	s_addc_u32 s27, s53, 0
	s_add_u32 s28, s52, 0x4c00
	s_addc_u32 s29, s53, 0
	s_add_u32 s30, s52, 0x4d00
	s_addc_u32 s31, s53, 0
	s_add_u32 s34, s52, 0x4e00
	s_addc_u32 s35, s53, 0
	s_add_u32 s36, s52, 0x4f00
	v_readlane_b32 s4, v254, 4
	s_addc_u32 s37, s53, 0
	v_readlane_b32 s5, v254, 5
	s_add_u32 s38, s52, 0x5000
	s_load_dwordx2 s[0:1], s[4:5], 0x4
	s_addc_u32 s39, s53, 0
	s_add_u32 s40, s52, 0x5100
	s_addc_u32 s41, s53, 0
	s_add_u32 s42, s52, 0x5200
	s_addc_u32 s43, s53, 0
	s_waitcnt lgkmcnt(0)
	s_mul_i32 s0, s0, s97
	s_add_u32 s44, s52, 0x5300
	s_mul_i32 s0, s0, s1
	s_addc_u32 s45, s53, 0
	s_mov_b32 s1, 1
	v_mov_b32_e32 v17, 0
	s_branch .LBB0_2238
